# conversion item: loads consumed as they land (progressive waits); otherwise as the previous version
# speedup vs baseline: 1.0018x; 1.0018x over previous
.Lcvt_common:
	v_lshlrev_b32_e32 v6, s16, v4
	v_lshl_add_u32 v6, v5, 4, v6
	s_waitcnt lgkmcnt(0)
	s_add_u32 s10, s10, s20
	s_addc_u32 s11, s11, s21
	s_add_i32 s17, s16, 7
	s_lshl_b32 s17, s12, s17
	s_add_u32 s10, s10, s17
	s_addc_u32 s11, s11, 0
	s_lshl_b32 s17, s13, 7
	s_add_u32 s10, s10, s17
	s_addc_u32 s11, s11, 0
	s_add_i32 s17, s16, 3
	s_lshl_b32 s17, 1, s17
	global_load_dwordx4 v[16:19], v6, s[10:11] nt
	s_add_u32 s10, s10, s17
	s_addc_u32 s11, s11, 0
	global_load_dwordx4 v[20:23], v6, s[10:11] nt
	s_add_u32 s10, s10, s17
	s_addc_u32 s11, s11, 0
	global_load_dwordx4 v[24:27], v6, s[10:11] nt
	s_add_u32 s10, s10, s17
	s_addc_u32 s11, s11, 0
	global_load_dwordx4 v[28:31], v6, s[10:11] nt
	s_add_u32 s10, s10, s17
	s_addc_u32 s11, s11, 0
	global_load_dwordx4 v[32:35], v6, s[10:11] nt
	s_add_u32 s10, s10, s17
	s_addc_u32 s11, s11, 0
	global_load_dwordx4 v[36:39], v6, s[10:11] nt
	s_add_u32 s10, s10, s17
	s_addc_u32 s11, s11, 0
	global_load_dwordx4 v[40:43], v6, s[10:11] nt
	s_add_u32 s10, s10, s17
	s_addc_u32 s11, s11, 0
	global_load_dwordx4 v[44:47], v6, s[10:11] nt
	s_add_u32 s10, s10, s17
	s_addc_u32 s11, s11, 0
	global_load_dwordx4 v[48:51], v6, s[10:11] nt
	s_add_u32 s10, s10, s17
	s_addc_u32 s11, s11, 0
	global_load_dwordx4 v[52:55], v6, s[10:11] nt
	s_add_u32 s10, s10, s17
	s_addc_u32 s11, s11, 0
	global_load_dwordx4 v[56:59], v6, s[10:11] nt
	s_add_u32 s10, s10, s17
	s_addc_u32 s11, s11, 0
	global_load_dwordx4 v[60:63], v6, s[10:11] nt
	s_add_u32 s10, s10, s17
	s_addc_u32 s11, s11, 0
	global_load_dwordx4 v[64:67], v6, s[10:11] nt
	s_add_u32 s10, s10, s17
	s_addc_u32 s11, s11, 0
	global_load_dwordx4 v[68:71], v6, s[10:11] nt
	s_add_u32 s10, s10, s17
	s_addc_u32 s11, s11, 0
	global_load_dwordx4 v[72:75], v6, s[10:11] nt
	s_add_u32 s10, s10, s17
	s_addc_u32 s11, s11, 0
	global_load_dwordx4 v[76:79], v6, s[10:11] nt
	s_add_u32 s22, s22, s2
	s_addc_u32 s23, s23, s3
	s_add_u32 s22, s22, s24
	s_addc_u32 s23, s23, 0
	s_lshl_b32 s17, s14, 15
	s_add_u32 s22, s22, s17
	s_addc_u32 s23, s23, 0
	s_lshl_b32 s17, s12, 7
	s_add_u32 s22, s22, s17
	s_addc_u32 s23, s23, 0
	s_mov_b32 s28, 0x0f0f0f0f
	s_mov_b32 s29, 0x0f0f0f0f
	s_mov_b64 exec, s[28:29]
	s_waitcnt vmcnt(15)
	v_mul_f32_e32 v80, 0x42000000, v16
	v_mul_f32_e32 v81, 0x42000000, v17
	v_mul_f32_e32 v82, 0x42000000, v18
	v_mul_f32_e32 v83, 0x42000000, v19
	ds_write_b32 v7, v80 offset:0
	ds_write_b32 v7, v81 offset:4
	ds_write_b32 v7, v82 offset:8
	ds_write_b32 v7, v83 offset:12
	s_waitcnt vmcnt(14)
	v_mul_f32_e32 v80, 0x42000000, v20
	v_mul_f32_e32 v81, 0x42000000, v21
	v_mul_f32_e32 v82, 0x42000000, v22
	v_mul_f32_e32 v83, 0x42000000, v23
	ds_write_b32 v7, v80 offset:544
	ds_write_b32 v7, v81 offset:548
	ds_write_b32 v7, v82 offset:552
	ds_write_b32 v7, v83 offset:556
	s_waitcnt vmcnt(13)
	v_mul_f32_e32 v80, 0x42000000, v24
	v_mul_f32_e32 v81, 0x42000000, v25
	v_mul_f32_e32 v82, 0x42000000, v26
	v_mul_f32_e32 v83, 0x42000000, v27
	ds_write_b32 v7, v80 offset:1088
	ds_write_b32 v7, v81 offset:1092
	ds_write_b32 v7, v82 offset:1096
	ds_write_b32 v7, v83 offset:1100
	s_waitcnt vmcnt(12)
	v_mul_f32_e32 v80, 0x42000000, v28
	v_mul_f32_e32 v81, 0x42000000, v29
	v_mul_f32_e32 v82, 0x42000000, v30
	v_mul_f32_e32 v83, 0x42000000, v31
	ds_write_b32 v7, v80 offset:1632
	ds_write_b32 v7, v81 offset:1636
	ds_write_b32 v7, v82 offset:1640
	ds_write_b32 v7, v83 offset:1644
	s_waitcnt vmcnt(11)
	v_mul_f32_e32 v80, 0x42000000, v32
	v_mul_f32_e32 v81, 0x42000000, v33
	v_mul_f32_e32 v82, 0x42000000, v34
	v_mul_f32_e32 v83, 0x42000000, v35
	ds_write_b32 v7, v80 offset:2176
	ds_write_b32 v7, v81 offset:2180
	ds_write_b32 v7, v82 offset:2184
	ds_write_b32 v7, v83 offset:2188
	s_waitcnt vmcnt(10)
	v_mul_f32_e32 v80, 0x42000000, v36
	v_mul_f32_e32 v81, 0x42000000, v37
	v_mul_f32_e32 v82, 0x42000000, v38
	v_mul_f32_e32 v83, 0x42000000, v39
	ds_write_b32 v7, v80 offset:2720
	ds_write_b32 v7, v81 offset:2724
	ds_write_b32 v7, v82 offset:2728
	ds_write_b32 v7, v83 offset:2732
	s_waitcnt vmcnt(9)
	v_mul_f32_e32 v80, 0x42000000, v40
	v_mul_f32_e32 v81, 0x42000000, v41
	v_mul_f32_e32 v82, 0x42000000, v42
	v_mul_f32_e32 v83, 0x42000000, v43
	ds_write_b32 v7, v80 offset:3264
	ds_write_b32 v7, v81 offset:3268
	ds_write_b32 v7, v82 offset:3272
	ds_write_b32 v7, v83 offset:3276
	s_waitcnt vmcnt(8)
	v_mul_f32_e32 v80, 0x42000000, v44
	v_mul_f32_e32 v81, 0x42000000, v45
	v_mul_f32_e32 v82, 0x42000000, v46
	v_mul_f32_e32 v83, 0x42000000, v47
	ds_write_b32 v7, v80 offset:3808
	ds_write_b32 v7, v81 offset:3812
	ds_write_b32 v7, v82 offset:3816
	ds_write_b32 v7, v83 offset:3820
	s_waitcnt vmcnt(7)
	v_mul_f32_e32 v80, 0x42000000, v48
	v_mul_f32_e32 v81, 0x42000000, v49
	v_mul_f32_e32 v82, 0x42000000, v50
	v_mul_f32_e32 v83, 0x42000000, v51
	ds_write_b32 v7, v80 offset:4352
	ds_write_b32 v7, v81 offset:4356
	ds_write_b32 v7, v82 offset:4360
	ds_write_b32 v7, v83 offset:4364
	s_waitcnt vmcnt(6)
	v_mul_f32_e32 v80, 0x42000000, v52
	v_mul_f32_e32 v81, 0x42000000, v53
	v_mul_f32_e32 v82, 0x42000000, v54
	v_mul_f32_e32 v83, 0x42000000, v55
	ds_write_b32 v7, v80 offset:4896
	ds_write_b32 v7, v81 offset:4900
	ds_write_b32 v7, v82 offset:4904
	ds_write_b32 v7, v83 offset:4908
	s_waitcnt vmcnt(5)
	v_mul_f32_e32 v80, 0x42000000, v56
	v_mul_f32_e32 v81, 0x42000000, v57
	v_mul_f32_e32 v82, 0x42000000, v58
	v_mul_f32_e32 v83, 0x42000000, v59
	ds_write_b32 v7, v80 offset:5440
	ds_write_b32 v7, v81 offset:5444
	ds_write_b32 v7, v82 offset:5448
	ds_write_b32 v7, v83 offset:5452
	s_waitcnt vmcnt(4)
	v_mul_f32_e32 v80, 0x42000000, v60
	v_mul_f32_e32 v81, 0x42000000, v61
	v_mul_f32_e32 v82, 0x42000000, v62
	v_mul_f32_e32 v83, 0x42000000, v63
	ds_write_b32 v7, v80 offset:5984
	ds_write_b32 v7, v81 offset:5988
	ds_write_b32 v7, v82 offset:5992
	ds_write_b32 v7, v83 offset:5996
	s_waitcnt vmcnt(3)
	v_mul_f32_e32 v80, 0x42000000, v64
	v_mul_f32_e32 v81, 0x42000000, v65
	v_mul_f32_e32 v82, 0x42000000, v66
	v_mul_f32_e32 v83, 0x42000000, v67
	ds_write_b32 v7, v80 offset:6528
	ds_write_b32 v7, v81 offset:6532
	ds_write_b32 v7, v82 offset:6536
	ds_write_b32 v7, v83 offset:6540
	s_waitcnt vmcnt(2)
	v_mul_f32_e32 v80, 0x42000000, v68
	v_mul_f32_e32 v81, 0x42000000, v69
	v_mul_f32_e32 v82, 0x42000000, v70
	v_mul_f32_e32 v83, 0x42000000, v71
	ds_write_b32 v7, v80 offset:7072
	ds_write_b32 v7, v81 offset:7076
	ds_write_b32 v7, v82 offset:7080
	ds_write_b32 v7, v83 offset:7084
	s_waitcnt vmcnt(1)
	v_mul_f32_e32 v80, 0x42000000, v72
	v_mul_f32_e32 v81, 0x42000000, v73
	v_mul_f32_e32 v82, 0x42000000, v74
	v_mul_f32_e32 v83, 0x42000000, v75
	ds_write_b32 v7, v80 offset:7616
	ds_write_b32 v7, v81 offset:7620
	ds_write_b32 v7, v82 offset:7624
	ds_write_b32 v7, v83 offset:7628
	s_waitcnt vmcnt(0)
	v_mul_f32_e32 v80, 0x42000000, v76
	v_mul_f32_e32 v81, 0x42000000, v77
	v_mul_f32_e32 v82, 0x42000000, v78
	v_mul_f32_e32 v83, 0x42000000, v79
	ds_write_b32 v7, v80 offset:8160
	ds_write_b32 v7, v81 offset:8164
	ds_write_b32 v7, v82 offset:8168
	ds_write_b32 v7, v83 offset:8172
	s_mov_b64 exec, -1
	s_waitcnt lgkmcnt(0)
	ds_read_b32 v84, v8 offset:0
	ds_read_b32 v85, v8 offset:68
	ds_read_b32 v86, v8 offset:136
	ds_read_b32 v87, v8 offset:204
	ds_read_b32 v88, v8 offset:272
	ds_read_b32 v89, v8 offset:340
	ds_read_b32 v90, v8 offset:408
	ds_read_b32 v91, v8 offset:476
	ds_read_b32 v92, v8 offset:544
	ds_read_b32 v93, v8 offset:612
	ds_read_b32 v94, v8 offset:680
	ds_read_b32 v95, v8 offset:748
	ds_read_b32 v96, v8 offset:816
	ds_read_b32 v97, v8 offset:884
	ds_read_b32 v98, v8 offset:952
	ds_read_b32 v99, v8 offset:1020
	s_waitcnt lgkmcnt(0)
	v_cvt_pk_fp8_f32 v100, v84, v85
	s_nop 0
	v_cvt_pk_fp8_f32 v100, v86, v87 op_sel:[0,0,1]
	v_cvt_pk_fp8_f32 v101, v88, v89
	s_nop 0
	v_cvt_pk_fp8_f32 v101, v90, v91 op_sel:[0,0,1]
	v_cvt_pk_fp8_f32 v102, v92, v93
	s_nop 0
	v_cvt_pk_fp8_f32 v102, v94, v95 op_sel:[0,0,1]
	v_cvt_pk_fp8_f32 v103, v96, v97
	s_nop 0
	v_cvt_pk_fp8_f32 v103, v98, v99 op_sel:[0,0,1]
	s_nop 0
	global_store_dwordx4 v9, v[100:103], s[22:23]
	s_nop 1
	ds_read_b32 v84, v8 offset:32
	ds_read_b32 v85, v8 offset:100
	ds_read_b32 v86, v8 offset:168
	ds_read_b32 v87, v8 offset:236
	ds_read_b32 v88, v8 offset:304
	ds_read_b32 v89, v8 offset:372
	ds_read_b32 v90, v8 offset:440
	ds_read_b32 v91, v8 offset:508
	ds_read_b32 v92, v8 offset:576
	ds_read_b32 v93, v8 offset:644
	ds_read_b32 v94, v8 offset:712
	ds_read_b32 v95, v8 offset:780
	ds_read_b32 v96, v8 offset:848
	ds_read_b32 v97, v8 offset:916
	ds_read_b32 v98, v8 offset:984
	ds_read_b32 v99, v8 offset:1052
	s_waitcnt lgkmcnt(0)
	v_cvt_pk_fp8_f32 v100, v84, v85
	s_nop 0
	v_cvt_pk_fp8_f32 v100, v86, v87 op_sel:[0,0,1]
	v_cvt_pk_fp8_f32 v101, v88, v89
	s_nop 0
	v_cvt_pk_fp8_f32 v101, v90, v91 op_sel:[0,0,1]
	v_cvt_pk_fp8_f32 v102, v92, v93
	s_nop 0
	v_cvt_pk_fp8_f32 v102, v94, v95 op_sel:[0,0,1]
	v_cvt_pk_fp8_f32 v103, v96, v97
	s_nop 0
	v_cvt_pk_fp8_f32 v103, v98, v99 op_sel:[0,0,1]
	s_nop 0
	global_store_dwordx4 v10, v[100:103], s[22:23]
	s_nop 1
	s_waitcnt lgkmcnt(0)
	s_not_b64 s[28:29], s[28:29]
	s_add_u32 s22, s22, 0x4000
	s_addc_u32 s23, s23, 0
	s_mov_b64 exec, s[28:29]
	v_mul_f32_e32 v80, 0x42000000, v16
	v_mul_f32_e32 v81, 0x42000000, v17
	v_mul_f32_e32 v82, 0x42000000, v18
	v_mul_f32_e32 v83, 0x42000000, v19
	ds_write_b32 v7, v80 offset:0
	ds_write_b32 v7, v81 offset:4
	ds_write_b32 v7, v82 offset:8
	ds_write_b32 v7, v83 offset:12
	v_mul_f32_e32 v80, 0x42000000, v20
	v_mul_f32_e32 v81, 0x42000000, v21
	v_mul_f32_e32 v82, 0x42000000, v22
	v_mul_f32_e32 v83, 0x42000000, v23
	ds_write_b32 v7, v80 offset:544
	ds_write_b32 v7, v81 offset:548
	ds_write_b32 v7, v82 offset:552
	ds_write_b32 v7, v83 offset:556
	v_mul_f32_e32 v80, 0x42000000, v24
	v_mul_f32_e32 v81, 0x42000000, v25
	v_mul_f32_e32 v82, 0x42000000, v26
	v_mul_f32_e32 v83, 0x42000000, v27
	ds_write_b32 v7, v80 offset:1088
	ds_write_b32 v7, v81 offset:1092
	ds_write_b32 v7, v82 offset:1096
	ds_write_b32 v7, v83 offset:1100
	v_mul_f32_e32 v80, 0x42000000, v28
	v_mul_f32_e32 v81, 0x42000000, v29
	v_mul_f32_e32 v82, 0x42000000, v30
	v_mul_f32_e32 v83, 0x42000000, v31
	ds_write_b32 v7, v80 offset:1632
	ds_write_b32 v7, v81 offset:1636
	ds_write_b32 v7, v82 offset:1640
	ds_write_b32 v7, v83 offset:1644
	v_mul_f32_e32 v80, 0x42000000, v32
	v_mul_f32_e32 v81, 0x42000000, v33
	v_mul_f32_e32 v82, 0x42000000, v34
	v_mul_f32_e32 v83, 0x42000000, v35
	ds_write_b32 v7, v80 offset:2176
	ds_write_b32 v7, v81 offset:2180
	ds_write_b32 v7, v82 offset:2184
	ds_write_b32 v7, v83 offset:2188
	v_mul_f32_e32 v80, 0x42000000, v36
	v_mul_f32_e32 v81, 0x42000000, v37
	v_mul_f32_e32 v82, 0x42000000, v38
	v_mul_f32_e32 v83, 0x42000000, v39
	ds_write_b32 v7, v80 offset:2720
	ds_write_b32 v7, v81 offset:2724
	ds_write_b32 v7, v82 offset:2728
	ds_write_b32 v7, v83 offset:2732
	v_mul_f32_e32 v80, 0x42000000, v40
	v_mul_f32_e32 v81, 0x42000000, v41
	v_mul_f32_e32 v82, 0x42000000, v42
	v_mul_f32_e32 v83, 0x42000000, v43
	ds_write_b32 v7, v80 offset:3264
	ds_write_b32 v7, v81 offset:3268
	ds_write_b32 v7, v82 offset:3272
	ds_write_b32 v7, v83 offset:3276
	v_mul_f32_e32 v80, 0x42000000, v44
	v_mul_f32_e32 v81, 0x42000000, v45
	v_mul_f32_e32 v82, 0x42000000, v46
	v_mul_f32_e32 v83, 0x42000000, v47
	ds_write_b32 v7, v80 offset:3808
	ds_write_b32 v7, v81 offset:3812
	ds_write_b32 v7, v82 offset:3816
	ds_write_b32 v7, v83 offset:3820
	v_mul_f32_e32 v80, 0x42000000, v48
	v_mul_f32_e32 v81, 0x42000000, v49
	v_mul_f32_e32 v82, 0x42000000, v50
	v_mul_f32_e32 v83, 0x42000000, v51
	ds_write_b32 v7, v80 offset:4352
	ds_write_b32 v7, v81 offset:4356
	ds_write_b32 v7, v82 offset:4360
	ds_write_b32 v7, v83 offset:4364
	v_mul_f32_e32 v80, 0x42000000, v52
	v_mul_f32_e32 v81, 0x42000000, v53
	v_mul_f32_e32 v82, 0x42000000, v54
	v_mul_f32_e32 v83, 0x42000000, v55
	ds_write_b32 v7, v80 offset:4896
	ds_write_b32 v7, v81 offset:4900
	ds_write_b32 v7, v82 offset:4904
	ds_write_b32 v7, v83 offset:4908
	v_mul_f32_e32 v80, 0x42000000, v56
	v_mul_f32_e32 v81, 0x42000000, v57
	v_mul_f32_e32 v82, 0x42000000, v58
	v_mul_f32_e32 v83, 0x42000000, v59
	ds_write_b32 v7, v80 offset:5440
	ds_write_b32 v7, v81 offset:5444
	ds_write_b32 v7, v82 offset:5448
	ds_write_b32 v7, v83 offset:5452
	v_mul_f32_e32 v80, 0x42000000, v60
	v_mul_f32_e32 v81, 0x42000000, v61
	v_mul_f32_e32 v82, 0x42000000, v62
	v_mul_f32_e32 v83, 0x42000000, v63
	ds_write_b32 v7, v80 offset:5984
	ds_write_b32 v7, v81 offset:5988
	ds_write_b32 v7, v82 offset:5992
	ds_write_b32 v7, v83 offset:5996
	v_mul_f32_e32 v80, 0x42000000, v64
	v_mul_f32_e32 v81, 0x42000000, v65
	v_mul_f32_e32 v82, 0x42000000, v66
	v_mul_f32_e32 v83, 0x42000000, v67
	ds_write_b32 v7, v80 offset:6528
	ds_write_b32 v7, v81 offset:6532
	ds_write_b32 v7, v82 offset:6536
	ds_write_b32 v7, v83 offset:6540
	v_mul_f32_e32 v80, 0x42000000, v68
	v_mul_f32_e32 v81, 0x42000000, v69
	v_mul_f32_e32 v82, 0x42000000, v70
	v_mul_f32_e32 v83, 0x42000000, v71
	ds_write_b32 v7, v80 offset:7072
	ds_write_b32 v7, v81 offset:7076
	ds_write_b32 v7, v82 offset:7080
	ds_write_b32 v7, v83 offset:7084
	v_mul_f32_e32 v80, 0x42000000, v72
	v_mul_f32_e32 v81, 0x42000000, v73
	v_mul_f32_e32 v82, 0x42000000, v74
	v_mul_f32_e32 v83, 0x42000000, v75
	ds_write_b32 v7, v80 offset:7616
	ds_write_b32 v7, v81 offset:7620
	ds_write_b32 v7, v82 offset:7624
	ds_write_b32 v7, v83 offset:7628
	v_mul_f32_e32 v80, 0x42000000, v76
	v_mul_f32_e32 v81, 0x42000000, v77
	v_mul_f32_e32 v82, 0x42000000, v78
	v_mul_f32_e32 v83, 0x42000000, v79
	ds_write_b32 v7, v80 offset:8160
	ds_write_b32 v7, v81 offset:8164
	ds_write_b32 v7, v82 offset:8168
	ds_write_b32 v7, v83 offset:8172
	s_mov_b64 exec, -1
	s_waitcnt lgkmcnt(0)
	ds_read_b32 v84, v8 offset:0
	ds_read_b32 v85, v8 offset:68
	ds_read_b32 v86, v8 offset:136
	ds_read_b32 v87, v8 offset:204
	ds_read_b32 v88, v8 offset:272
	ds_read_b32 v89, v8 offset:340
	ds_read_b32 v90, v8 offset:408
	ds_read_b32 v91, v8 offset:476
	ds_read_b32 v92, v8 offset:544
	ds_read_b32 v93, v8 offset:612
	ds_read_b32 v94, v8 offset:680
	ds_read_b32 v95, v8 offset:748
	ds_read_b32 v96, v8 offset:816
	ds_read_b32 v97, v8 offset:884
	ds_read_b32 v98, v8 offset:952
	ds_read_b32 v99, v8 offset:1020
	s_waitcnt lgkmcnt(0)
	v_cvt_pk_fp8_f32 v100, v84, v85
	s_nop 0
	v_cvt_pk_fp8_f32 v100, v86, v87 op_sel:[0,0,1]
	v_cvt_pk_fp8_f32 v101, v88, v89
	s_nop 0
	v_cvt_pk_fp8_f32 v101, v90, v91 op_sel:[0,0,1]
	v_cvt_pk_fp8_f32 v102, v92, v93
	s_nop 0
	v_cvt_pk_fp8_f32 v102, v94, v95 op_sel:[0,0,1]
	v_cvt_pk_fp8_f32 v103, v96, v97
	s_nop 0
	v_cvt_pk_fp8_f32 v103, v98, v99 op_sel:[0,0,1]
	s_nop 0
	global_store_dwordx4 v9, v[100:103], s[22:23]
	s_nop 1
	ds_read_b32 v84, v8 offset:32
	ds_read_b32 v85, v8 offset:100
	ds_read_b32 v86, v8 offset:168
	ds_read_b32 v87, v8 offset:236
	ds_read_b32 v88, v8 offset:304
	ds_read_b32 v89, v8 offset:372
	ds_read_b32 v90, v8 offset:440
	ds_read_b32 v91, v8 offset:508
	ds_read_b32 v92, v8 offset:576
	ds_read_b32 v93, v8 offset:644
	ds_read_b32 v94, v8 offset:712
	ds_read_b32 v95, v8 offset:780
	ds_read_b32 v96, v8 offset:848
	ds_read_b32 v97, v8 offset:916
	ds_read_b32 v98, v8 offset:984
	ds_read_b32 v99, v8 offset:1052
	s_waitcnt lgkmcnt(0)
	v_cvt_pk_fp8_f32 v100, v84, v85
	s_nop 0
	v_cvt_pk_fp8_f32 v100, v86, v87 op_sel:[0,0,1]
	v_cvt_pk_fp8_f32 v101, v88, v89
	s_nop 0
	v_cvt_pk_fp8_f32 v101, v90, v91 op_sel:[0,0,1]
	v_cvt_pk_fp8_f32 v102, v92, v93
	s_nop 0
	v_cvt_pk_fp8_f32 v102, v94, v95 op_sel:[0,0,1]
	v_cvt_pk_fp8_f32 v103, v96, v97
	s_nop 0
	v_cvt_pk_fp8_f32 v103, v98, v99 op_sel:[0,0,1]
	s_nop 0
	global_store_dwordx4 v10, v[100:103], s[22:23]
	s_nop 1
	s_add_i32 s30, s30, 1
	s_add_i32 s26, s26, -1
	s_cmp_lg_u32 s26, 0
	s_cbranch_scc1 .Lcvt_item
